# GEMM unit headers: division by the row-group size becomes a shift when the group size is 8 (skips the VALU reciprocal + readfirstlane sequence)
# speedup vs baseline: 1.0035x; 1.0035x over previous
.LBB0_299:
	s_add_i32 s84, s84, 1
	s_mul_i32 s0, s84, s69
	s_mul_hi_u32 s1, s84, s68
	s_add_i32 s1, s1, s0
	s_mul_i32 s0, s84, s68
	s_add_u32 s0, s0, s36
	s_addc_u32 s1, s1, s62
	v_mov_b64_e32 v[2:3], s[20:21]
	v_cmp_ge_i64_e64 s[38:39], s[0:1], v[2:3]
	s_and_b64 vcc, exec, s[38:39]
	s_cbranch_vccnz .LBB0_301
	s_ashr_i32 s1, s0, 31
	s_lshr_b32 s1, s1, 29
	s_add_i32 s1, s0, s1
	s_ashr_i32 s14, s1, 3
	s_and_b32 s1, s1, -8
	s_sub_i32 s0, s0, s1
	s_cmp_lt_i32 s0, 0
	s_cselect_b32 s1, s63, s59
	s_mul_i32 s0, s0, s1
	s_add_i32 s0, s0, s14
	s_abs_i32 s14, s0
	s_mul_hi_u32 s15, s14, s73
	s_mul_i32 s28, s15, s65
	s_ashr_i32 s1, s0, 31
	s_sub_i32 s14, s14, s28
	s_xor_b32 s1, s1, s72
	s_add_i32 s28, s15, 1
	s_sub_i32 s29, s14, s65
	s_cmp_ge_u32 s14, s65
	s_cselect_b32 s15, s28, s15
	s_cselect_b32 s14, s29, s14
	s_add_i32 s28, s15, 1
	s_cmp_ge_u32 s14, s65
	s_cselect_b32 s14, s28, s15
	s_xor_b32 s14, s14, s1
	s_sub_i32 s1, s14, s1
	s_lshl_b32 s14, s1, 3
	s_sub_i32 s15, s70, s14
	s_min_i32 s15, s15, 8
	s_cmp_eq_u32 s15, 8
	s_cbranch_scc1 .Lgfast_0
	s_abs_i32 s28, s15
	v_cvt_f32_u32_e32 v2, s28
	s_sub_i32 s48, 0, s28
	s_mul_i32 s1, s1, s64
	s_sub_i32 s0, s0, s1
	v_rcp_iflag_f32_e32 v2, v2
	s_abs_i32 s29, s0
	s_xor_b32 s1, s0, s15
	s_ashr_i32 s1, s1, 31
	v_mul_f32_e32 v2, 0x4f7ffffe, v2
	v_cvt_u32_f32_e32 v2, v2
	s_nop 0
	v_readfirstlane_b32 s49, v2
	s_mul_i32 s48, s48, s49
	s_mul_hi_u32 s48, s49, s48
	s_add_i32 s49, s49, s48
	s_mul_hi_u32 s48, s29, s49
	s_mul_i32 s49, s48, s28
	s_sub_i32 s29, s29, s49
	s_add_i32 s49, s48, 1
	s_sub_i32 s50, s29, s28
	s_cmp_ge_u32 s29, s28
	s_cselect_b32 s48, s49, s48
	s_cselect_b32 s29, s50, s29
	s_add_i32 s49, s48, 1
	s_cmp_ge_u32 s29, s28
	s_cselect_b32 s28, s49, s48
	s_xor_b32 s28, s28, s1
	s_sub_i32 s85, s28, s1
	s_branch .Lgdone_0
.Lgfast_0:
	s_mul_i32 s1, s1, s64
	s_sub_i32 s0, s0, s1
	s_ashr_i32 s85, s0, 3
.Lgdone_0:
	s_mul_i32 s1, s85, s15
	s_sub_i32 s0, s0, s1
	s_add_i32 s86, s0, s14
	s_lshl_b32 s0, s86, 8
	s_add_i32 s0, s0, s13
	s_ashr_i32 s1, s0, 31
	s_lshl_b64 s[0:1], s[0:1], 11
	s_add_u32 s48, s54, s0
	s_addc_u32 s49, s55, s1
	s_lshl_b32 s0, s85, 8
	s_ashr_i32 s1, s0, 31
	s_lshl_b64 s[0:1], s[0:1], 11
	s_add_u32 s50, s56, s0
	s_addc_u32 s51, s57, s1

.LBB0_993:
	s_add_i32 s72, s72, 1
	s_mul_i32 s0, s72, s69
	s_mul_hi_u32 s1, s72, s68
	s_add_i32 s1, s1, s0
	s_mul_i32 s0, s72, s68
	s_add_u32 s0, s0, s53
	s_addc_u32 s1, s1, s47
	v_mov_b64_e32 v[2:3], s[20:21]
	v_cmp_ge_i64_e64 s[38:39], s[0:1], v[2:3]
	s_and_b64 vcc, exec, s[38:39]
	s_cbranch_vccnz .LBB0_995
	s_ashr_i32 s1, s0, 31
	s_lshr_b32 s1, s1, 29
	s_add_i32 s1, s0, s1
	s_ashr_i32 s2, s1, 3
	s_and_b32 s1, s1, -8
	s_sub_i32 s0, s0, s1
	s_cmp_lt_i32 s0, 0
	s_cselect_b32 s1, s48, s46
	s_mul_i32 s0, s0, s1
	s_add_i32 s0, s0, s2
	s_ashr_i32 s1, s0, 31
	s_lshr_b32 s1, s1, 27
	s_add_i32 s1, s0, s1
	s_ashr_i32 s2, s1, 5
	s_lshl_b32 s2, s2, 3
	s_sub_i32 s3, s70, s2
	s_min_i32 s3, s3, 8
	s_cmp_eq_u32 s3, 8
	s_cbranch_scc1 .Lgfast_1
	s_abs_i32 s18, s3
	v_cvt_f32_u32_e32 v2, s18
	s_waitcnt lgkmcnt(0)
	s_sub_i32 s42, 0, s18
	s_andn2_b32 s1, s1, 31
	s_sub_i32 s0, s0, s1
	v_rcp_iflag_f32_e32 v2, v2
	s_abs_i32 s1, s0
	s_xor_b32 s19, s0, s3
	s_ashr_i32 s19, s19, 31
	v_mul_f32_e32 v2, 0x4f7ffffe, v2
	v_cvt_u32_f32_e32 v2, v2
	s_nop 0
	v_readfirstlane_b32 s43, v2
	s_mul_i32 s42, s42, s43
	s_mul_hi_u32 s42, s43, s42
	s_add_i32 s43, s43, s42
	s_mul_hi_u32 s42, s1, s43
	s_mul_i32 s43, s42, s18
	s_sub_i32 s1, s1, s43
	s_add_i32 s44, s42, 1
	s_sub_i32 s43, s1, s18
	s_cmp_ge_u32 s1, s18
	s_cselect_b32 s42, s44, s42
	s_cselect_b32 s1, s43, s1
	s_add_i32 s43, s42, 1
	s_cmp_ge_u32 s1, s18
	s_cselect_b32 s1, s43, s42
	s_xor_b32 s1, s1, s19
	s_sub_i32 s73, s1, s19
	s_branch .Lgdone_1
.Lgfast_1:
	s_waitcnt lgkmcnt(0)
	s_andn2_b32 s1, s1, 31
	s_sub_i32 s0, s0, s1
	s_ashr_i32 s73, s0, 3
.Lgdone_1:
	s_mul_i32 s1, s73, s3
	s_sub_i32 s0, s0, s1
	s_add_i32 s76, s2, s0
	s_lshl_b32 s0, s76, 8
	s_add_i32 s0, s0, s13
	s_ashr_i32 s1, s0, 31
	s_lshl_b64 s[0:1], s[0:1], 10
	s_add_u32 s2, s54, s0
	s_addc_u32 s3, s55, s1
	s_lshl_b32 s0, s73, 8
	s_ashr_i32 s1, s0, 31
	s_lshl_b64 s[0:1], s[0:1], 10
	s_add_u32 s18, s15, s0
	s_addc_u32 s19, s16, s1

.LBB0_1008:
	s_add_i32 s80, s80, 1
	s_mul_i32 s0, s80, s69
	s_mul_hi_u32 s1, s80, s68
	s_add_i32 s1, s1, s0
	s_mul_i32 s0, s80, s68
	s_add_u32 s0, s0, s53
	s_addc_u32 s1, s1, s59
	v_mov_b64_e32 v[2:3], s[2:3]
	v_cmp_ge_i64_e64 s[38:39], s[0:1], v[2:3]
	s_and_b64 vcc, exec, s[38:39]
	s_cbranch_vccnz .LBB0_1010
	s_ashr_i32 s1, s0, 31
	s_lshr_b32 s1, s1, 29
	s_add_i32 s1, s0, s1
	s_ashr_i32 s14, s1, 3
	s_and_b32 s1, s1, -8
	s_sub_i32 s0, s0, s1
	s_cmp_lt_i32 s0, 0
	s_cselect_b32 s1, s62, s58
	s_mul_i32 s0, s0, s1
	s_add_i32 s0, s0, s14
	s_ashr_i32 s1, s0, 31
	s_lshr_b32 s1, s1, 27
	s_add_i32 s1, s0, s1
	s_ashr_i32 s14, s1, 5
	s_lshl_b32 s14, s14, 3
	s_sub_i32 s15, s70, s14
	s_min_i32 s15, s15, 8
	s_cmp_eq_u32 s15, 8
	s_cbranch_scc1 .Lgfast_2
	s_abs_i32 s20, s15
	v_cvt_f32_u32_e32 v2, s20
	s_sub_i32 s41, 0, s20
	s_andn2_b32 s1, s1, 31
	s_sub_i32 s0, s0, s1
	v_rcp_iflag_f32_e32 v2, v2
	s_abs_i32 s1, s0
	s_xor_b32 s40, s0, s15
	s_ashr_i32 s40, s40, 31
	v_mul_f32_e32 v2, 0x4f7ffffe, v2
	v_cvt_u32_f32_e32 v2, v2
	s_nop 0
	v_readfirstlane_b32 s42, v2
	s_mul_i32 s41, s41, s42
	s_mul_hi_u32 s41, s42, s41
	s_add_i32 s42, s42, s41
	s_mul_hi_u32 s41, s1, s42
	s_mul_i32 s42, s41, s20
	s_sub_i32 s1, s1, s42
	s_add_i32 s43, s41, 1
	s_sub_i32 s42, s1, s20
	s_cmp_ge_u32 s1, s20
	s_cselect_b32 s41, s43, s41
	s_cselect_b32 s1, s42, s1
	s_add_i32 s42, s41, 1
	s_cmp_ge_u32 s1, s20
	s_cselect_b32 s1, s42, s41
	s_xor_b32 s1, s1, s40
	s_sub_i32 s81, s1, s40
	s_branch .Lgdone_2
.Lgfast_2:
	s_andn2_b32 s1, s1, 31
	s_sub_i32 s0, s0, s1
	s_ashr_i32 s81, s0, 3
.Lgdone_2:
	s_mul_i32 s1, s81, s15
	s_sub_i32 s0, s0, s1
	s_add_i32 s82, s14, s0
	s_lshl_b32 s0, s82, 8
	s_add_i32 s0, s0, s13
	s_ashr_i32 s1, s0, 31
	s_lshl_b64 s[0:1], s[0:1], 11
	s_add_u32 s40, s54, s0
	s_addc_u32 s41, s55, s1
	s_lshl_b32 s0, s81, 8
	s_ashr_i32 s1, s0, 31
	s_lshl_b64 s[0:1], s[0:1], 11
	s_add_u32 s42, s17, s0
	s_addc_u32 s43, s56, s1

.LBB0_1245:
	s_ashr_i32 s0, s18, 3
	s_add_i32 s0, s42, s0
	s_ashr_i32 s1, s0, 31
	s_lshr_b32 s1, s1, 27
	s_add_i32 s1, s0, s1
	s_ashr_i32 s18, s1, 5
	s_lshl_b32 s18, s18, 3
	s_sub_i32 s19, s15, s18
	s_min_i32 s19, s19, 8
	s_cmp_eq_u32 s19, 8
	s_cbranch_scc1 .Lgfast_3
	s_abs_i32 s42, s19
	v_cvt_f32_u32_e32 v2, s42
	s_sub_i32 s44, 0, s42
	s_andn2_b32 s1, s1, 31
	s_sub_i32 s0, s0, s1
	v_rcp_iflag_f32_e32 v2, v2
	s_abs_i32 s1, s0
	s_xor_b32 s43, s0, s19
	s_ashr_i32 s43, s43, 31
	v_mul_f32_e32 v2, 0x4f7ffffe, v2
	v_cvt_u32_f32_e32 v2, v2
	s_nop 0
	v_readfirstlane_b32 s45, v2
	s_mul_i32 s44, s44, s45
	s_mul_hi_u32 s44, s45, s44
	s_add_i32 s45, s45, s44
	s_mul_hi_u32 s44, s1, s45
	s_mul_i32 s45, s44, s42
	s_sub_i32 s1, s1, s45
	s_add_i32 s46, s44, 1
	s_sub_i32 s45, s1, s42
	s_cmp_ge_u32 s1, s42
	s_cselect_b32 s44, s46, s44
	s_cselect_b32 s1, s45, s1
	s_add_i32 s45, s44, 1
	s_cmp_ge_u32 s1, s42
	s_cselect_b32 s1, s45, s44
	s_xor_b32 s1, s1, s43
	s_sub_i32 s73, s1, s43
	s_branch .Lgdone_3
.Lgfast_3:
	s_andn2_b32 s1, s1, 31
	s_sub_i32 s0, s0, s1
	s_ashr_i32 s73, s0, 3
.Lgdone_3:
	s_mul_i32 s1, s73, s19
	s_sub_i32 s0, s0, s1
	s_add_i32 s76, s18, s0
	s_lshl_b32 s0, s76, 2
	s_add_i32 s0, s0, 0
	s_add_i32 s0, s0, 0x23200
	v_mov_b32_e32 v2, s0
	ds_read_b32 v2, v2
	s_lshl_b32 s0, s73, 8
	s_ashr_i32 s1, s0, 31
	s_lshl_b64 s[0:1], s[0:1], 10
	s_waitcnt lgkmcnt(0)
	v_readfirstlane_b32 s18, v2
	s_ashr_i32 s19, s18, 31
	s_lshl_b64 s[18:19], s[18:19], 20
	s_add_u32 s18, s54, s18
	s_addc_u32 s19, s55, s19
	s_add_u32 s44, s18, s0
	s_addc_u32 s45, s19, s1

.LBB0_1337:
	s_ashr_i32 s0, s14, 3
	s_add_i32 s0, s18, s0
	s_ashr_i32 s1, s0, 31
	s_lshr_b32 s1, s1, 27
	s_add_i32 s1, s0, s1
	s_ashr_i32 s14, s1, 5
	s_lshl_b32 s14, s14, 3
	s_sub_i32 s15, s58, s14
	s_min_i32 s15, s15, 8
	s_cmp_eq_u32 s15, 8
	s_cbranch_scc1 .Lgfast_4
	s_abs_i32 s18, s15
	v_cvt_f32_u32_e32 v2, s18
	s_sub_i32 s28, 0, s18
	s_andn2_b32 s1, s1, 31
	s_sub_i32 s0, s0, s1
	v_rcp_iflag_f32_e32 v2, v2
	s_abs_i32 s1, s0
	s_xor_b32 s19, s0, s15
	s_ashr_i32 s19, s19, 31
	v_mul_f32_e32 v2, 0x4f7ffffe, v2
	v_cvt_u32_f32_e32 v2, v2
	s_nop 0
	v_readfirstlane_b32 s29, v2
	s_mul_i32 s28, s28, s29
	s_mul_hi_u32 s28, s29, s28
	s_add_i32 s29, s29, s28
	s_mul_hi_u32 s28, s1, s29
	s_mul_i32 s29, s28, s18
	s_sub_i32 s1, s1, s29
	s_add_i32 s36, s28, 1
	s_sub_i32 s29, s1, s18
	s_cmp_ge_u32 s1, s18
	s_cselect_b32 s28, s36, s28
	s_cselect_b32 s1, s29, s1
	s_add_i32 s29, s28, 1
	s_cmp_ge_u32 s1, s18
	s_cselect_b32 s1, s29, s28
	s_xor_b32 s1, s1, s19
	s_sub_i32 s83, s1, s19
	s_branch .Lgdone_4
.Lgfast_4:
	s_andn2_b32 s1, s1, 31
	s_sub_i32 s0, s0, s1
	s_ashr_i32 s83, s0, 3
.Lgdone_4:
	s_mul_i32 s1, s83, s15
	s_sub_i32 s0, s0, s1
	s_add_i32 s18, s14, s0
	s_lshl_b32 s0, s18, 2
	s_add_i32 s0, s0, 0
	s_add_i32 s0, s0, 0x23200
	v_mov_b32_e32 v2, s0
	ds_read_b32 v2, v2
	s_ashr_i32 s19, s18, 31
	s_lshl_b64 s[0:1], s[18:19], 17
	s_add_u32 s28, s70, s0
	s_addc_u32 s29, s71, s1
	s_lshl_b32 s0, s83, 8
	s_waitcnt lgkmcnt(0)
	v_readfirstlane_b32 s14, v2
	s_ashr_i32 s15, s14, 31
	s_ashr_i32 s1, s0, 31
	s_lshl_b64 s[14:15], s[14:15], 19
	s_lshl_b64 s[0:1], s[0:1], 9
	s_add_u32 s14, s72, s14
	s_addc_u32 s15, s73, s15
	s_add_u32 s36, s14, s0
	s_addc_u32 s37, s15, s1
